# speedup vs baseline: 1.0217x; 1.0217x over previous
.LBB1_3:
	s_load_dwordx8 s[4:11], s[0:1], 0x0
	v_lshrrev_b32_e32 v1, 6, v0
	v_mov_b32_e32 v3, 0
	v_lshl_or_b32 v2, s2, 2, v1
	v_lshlrev_b32_e32 v7, 12, v2
	s_waitcnt lgkmcnt(0)
	v_lshl_add_u64 v[4:5], v[2:3], 2, s[4:5]
	global_load_dword v6, v[4:5], off
	v_and_b32_e32 v8, 0x3ff000, v7
	v_and_b32_e32 v1, 63, v0
	v_mov_b32_e32 v9, v3
	v_lshlrev_b32_e32 v4, 4, v1
	v_mov_b32_e32 v5, v3
	v_lshl_add_u64 v[8:9], s[8:9], 0, v[8:9]
	v_lshl_add_u64 v[38:39], v[8:9], 0, v[4:5]
	s_mov_b32 s3, 0xf800000
	v_mov_b32_e32 v78, 0x260
	s_waitcnt vmcnt(0)
	v_ashrrev_i32_e32 v7, 31, v6
	v_lshlrev_b64 v[6:7], 12, v[6:7]
	v_lshl_add_u64 v[6:7], s[6:7], 0, v[6:7]
	v_lshl_add_u64 v[40:41], v[6:7], 0, v[4:5]
	global_load_dwordx4 v[6:9], v[40:41], off
	global_load_dwordx4 v[10:13], v[38:39], off
	global_load_dwordx4 v[14:17], v[38:39], off offset:1024
	global_load_dwordx4 v[18:21], v[40:41], off offset:1024
	global_load_dwordx4 v[22:25], v[40:41], off offset:2048
	global_load_dwordx4 v[26:29], v[38:39], off offset:2048
	global_load_dwordx4 v[30:33], v[38:39], off offset:3072
	global_load_dwordx4 v[34:37], v[40:41], off offset:3072
	v_mbcnt_lo_u32_b32 v38, -1, 0
	v_mbcnt_hi_u32_b32 v38, -1, v38
	v_and_b32_e32 v39, 64, v38
	v_xor_b32_e32 v40, 32, v38
	v_add_u32_e32 v39, 64, v39
	v_cmp_lt_i32_e32 vcc, v40, v39
	s_load_dwordx4 s[4:7], s[0:1], 0x20
	s_load_dwordx2 s[8:9], s[0:1], 0x30
	v_cndmask_b32_e32 v40, v38, v40, vcc
	v_lshlrev_b32_e32 v70, 2, v40
	s_waitcnt vmcnt(6)
	v_pk_add_f32 v[6:7], v[6:7], v[10:11]
	v_pk_add_f32 v[8:9], v[8:9], v[12:13]
	s_waitcnt vmcnt(4)
	v_pk_add_f32 v[10:11], v[18:19], v[14:15]
	v_pk_add_f32 v[12:13], v[20:21], v[16:17]
	s_waitcnt vmcnt(2)
	v_pk_add_f32 v[14:15], v[22:23], v[26:27]
	v_pk_add_f32 v[16:17], v[24:25], v[28:29]
	v_mov_b32_e32 v22, v6
	v_mov_b32_e32 v23, v8
	v_mov_b32_e32 v24, v7
	v_mov_b32_e32 v25, v9
	v_mov_b32_e32 v26, v10
	v_mov_b32_e32 v27, v12
	v_mov_b32_e32 v28, v11
	v_mov_b32_e32 v29, v13
	v_pk_add_f32 v[22:23], v[22:23], v[24:25]
	v_pk_add_f32 v[24:25], v[26:27], v[28:29]
	s_waitcnt vmcnt(0)
	v_pk_add_f32 v[18:19], v[34:35], v[30:31]
	v_pk_add_f32 v[20:21], v[36:37], v[32:33]
	v_pk_add_f32 v[30:31], v[14:15], v[14:15] op_sel:[0,1] op_sel_hi:[1,0]
	v_pk_add_f32 v[32:33], v[16:17], v[16:17] op_sel:[0,1] op_sel_hi:[1,0]
	v_add_f32_e32 v26, v22, v23
	v_pk_add_f32 v[22:23], v[24:25], v[24:25] op_sel:[0,1] op_sel_hi:[1,0]
	v_mov_b32_e32 v35, v18
	v_mov_b32_e32 v31, v20
	v_mov_b32_e32 v33, v21
	v_add_f32_e32 v34, 0, v26
	v_mov_b32_e32 v23, v19
	v_pk_add_f32 v[24:25], v[30:31], v[32:33]
	v_pk_add_f32 v[22:23], v[34:35], v[22:23]
	s_nop 0
	v_pk_add_f32 v[22:23], v[22:23], v[24:25]
	v_xor_b32_e32 v24, 16, v38
	v_add_f32_e32 v22, v22, v23
	v_mov_b32_e32 v23, v22
	v_cmp_lt_i32_e32 vcc, v24, v39
	s_waitcnt lgkmcnt(0)
	s_nop 1
	v_permlane32_swap_b32_e32 v22, v23
	v_add_f32_e32 v22, v22, v23
	v_cndmask_b32_e32 v24, v38, v24, vcc
	v_lshlrev_b32_e32 v71, 2, v24
	v_mov_b32_e32 v23, v22
	v_xor_b32_e32 v24, 8, v38
	v_cmp_lt_i32_e32 vcc, v24, v39
	s_waitcnt lgkmcnt(0)
	s_nop 1
	v_permlane16_swap_b32_e32 v22, v23
	v_add_f32_e32 v22, v22, v23
	v_cndmask_b32_e32 v24, v38, v24, vcc
	v_lshlrev_b32_e32 v72, 2, v24
	v_xor_b32_e32 v24, 4, v38
	v_cmp_lt_i32_e32 vcc, v24, v39
	s_waitcnt lgkmcnt(0)
	s_nop 1
	v_add_f32_dpp v22, v22, v22 row_ror:8 row_mask:0xf bank_mask:0xf
	v_cndmask_b32_e32 v24, v38, v24, vcc
	v_lshlrev_b32_e32 v73, 2, v24
	v_xor_b32_e32 v24, 2, v38
	v_cmp_lt_i32_e32 vcc, v24, v39
	s_waitcnt lgkmcnt(0)
	s_nop 1
	v_add_f32_dpp v22, v22, v22 row_ror:4 row_mask:0xf bank_mask:0xf
	v_cndmask_b32_e32 v24, v38, v24, vcc
	v_lshlrev_b32_e32 v74, 2, v24
	v_xor_b32_e32 v24, 1, v38
	v_cmp_lt_i32_e32 vcc, v24, v39
	s_nop 1
	v_cndmask_b32_e32 v24, v38, v24, vcc
	v_lshlrev_b32_e32 v75, 2, v24
	s_waitcnt lgkmcnt(0)
	s_nop 1
	v_add_f32_dpp v38, v22, v22 row_ror:2 row_mask:0xf bank_mask:0xf
	global_load_dwordx4 v[22:25], v4, s[4:5]
	global_load_dwordx4 v[26:29], v4, s[6:7]
	global_load_dwordx4 v[30:33], v4, s[4:5] offset:1024
	global_load_dwordx4 v[34:37], v4, s[6:7] offset:1024
	s_waitcnt lgkmcnt(0)
	s_nop 1
	v_add_f32_dpp v38, v38, v38 row_ror:1 row_mask:0xf bank_mask:0xf
	v_mul_f32_e32 v38, 0x3a800000, v38
	v_pk_add_f32 v[54:55], v[6:7], v[38:39] op_sel_hi:[1,0] neg_lo:[0,1] neg_hi:[0,1]
	v_pk_add_f32 v[56:57], v[8:9], v[38:39] op_sel_hi:[1,0] neg_lo:[0,1] neg_hi:[0,1]
	v_pk_add_f32 v[58:59], v[10:11], v[38:39] op_sel_hi:[1,0] neg_lo:[0,1] neg_hi:[0,1]
	v_pk_add_f32 v[60:61], v[12:13], v[38:39] op_sel_hi:[1,0] neg_lo:[0,1] neg_hi:[0,1]
	v_mov_b32_e32 v40, v55
	v_mov_b32_e32 v41, v57
	v_mov_b32_e32 v44, v59
	v_mov_b32_e32 v45, v61
	v_pk_add_f32 v[62:63], v[14:15], v[38:39] op_sel_hi:[1,0] neg_lo:[0,1] neg_hi:[0,1]
	v_pk_add_f32 v[64:65], v[16:17], v[38:39] op_sel_hi:[1,0] neg_lo:[0,1] neg_hi:[0,1]
	v_pk_add_f32 v[66:67], v[18:19], v[38:39] op_sel_hi:[1,0] neg_lo:[0,1] neg_hi:[0,1]
	v_pk_add_f32 v[68:69], v[20:21], v[38:39] op_sel_hi:[1,0] neg_lo:[0,1] neg_hi:[0,1]
	v_mov_b32_e32 v38, v54
	v_mov_b32_e32 v39, v56
	v_mov_b32_e32 v42, v58
	v_mov_b32_e32 v43, v60
	v_pk_mul_f32 v[40:41], v[40:41], v[40:41]
	v_pk_mul_f32 v[44:45], v[44:45], v[44:45]
	v_mul_f32_e32 v46, v62, v62
	v_mul_f32_e32 v48, v64, v64
	v_pk_fma_f32 v[38:39], v[38:39], v[38:39], v[40:41]
	v_pk_fma_f32 v[40:41], v[42:43], v[42:43], v[44:45]
	v_pk_mul_f32 v[50:51], v[66:67], v[66:67]
	v_pk_mul_f32 v[52:53], v[68:69], v[68:69]
	v_pk_fma_f32 v[46:47], v[62:63], v[62:63], v[46:47] op_sel_hi:[1,1,0]
	v_pk_fma_f32 v[48:49], v[64:65], v[64:65], v[48:49] op_sel_hi:[1,1,0]
	v_pk_add_f32 v[38:39], v[38:39], v[38:39] op_sel_hi:[0,1]
	v_pk_add_f32 v[40:41], v[40:41], v[40:41] op_sel_hi:[0,1]
	v_mov_b32_e32 v46, v50
	v_mov_b32_e32 v48, v51
	v_mov_b32_e32 v38, v52
	v_mov_b32_e32 v40, v53
	v_pk_add_f32 v[42:43], v[46:47], v[48:49]
	v_pk_add_f32 v[38:39], v[38:39], v[40:41]
	s_nop 0
	v_pk_add_f32 v[38:39], v[42:43], v[38:39]
	s_nop 0
	v_add_f32_e32 v76, v38, v39
	global_load_dwordx4 v[38:41], v4, s[4:5] offset:2048
	global_load_dwordx4 v[42:45], v4, s[6:7] offset:2048
	global_load_dwordx4 v[46:49], v4, s[4:5] offset:3072
	global_load_dwordx4 v[50:53], v4, s[6:7] offset:3072
	v_mov_b32_e32 v70, v76
	s_waitcnt lgkmcnt(0)
	s_nop 1
	v_permlane32_swap_b32_e32 v76, v70
	v_add_f32_e32 v70, v76, v70
	v_mov_b32_e32 v71, v70
	v_mov_b32_e32 v76, 0x3727c5ac
	s_waitcnt lgkmcnt(0)
	s_nop 1
	v_permlane16_swap_b32_e32 v70, v71
	v_add_f32_e32 v70, v70, v71
	s_waitcnt lgkmcnt(0)
	s_nop 1
	v_add_f32_dpp v70, v70, v70 row_ror:8 row_mask:0xf bank_mask:0xf
	v_lshlrev_b64 v[72:73], 11, v[2:3]
	v_lshl_add_u64 v[72:73], s[8:9], 0, v[72:73]
	s_waitcnt lgkmcnt(0)
	s_nop 1
	v_add_f32_dpp v77, v70, v70 row_ror:4 row_mask:0xf bank_mask:0xf
	v_lshlrev_b64 v[70:71], 12, v[2:3]
	v_lshlrev_b32_e32 v2, 3, v1
	v_lshl_add_u64 v[70:71], s[10:11], 0, v[70:71]
	v_lshl_add_u64 v[4:5], v[70:71], 0, v[4:5]
	s_waitcnt lgkmcnt(0)
	s_nop 1
	v_add_f32_dpp v74, v77, v77 row_ror:2 row_mask:0xf bank_mask:0xf
	global_store_dwordx4 v[4:5], v[6:9], off
	global_store_dwordx4 v[4:5], v[10:13], off offset:1024
	global_store_dwordx4 v[4:5], v[14:17], off offset:2048
	global_store_dwordx4 v[4:5], v[18:21], off offset:3072
	v_lshl_add_u64 v[2:3], v[72:73], 0, v[2:3]
	s_waitcnt lgkmcnt(0)
	s_nop 1
	v_add_f32_dpp v1, v74, v74 row_ror:1 row_mask:0xf bank_mask:0xf
	v_fmac_f32_e32 v76, 0x3a800000, v1
	v_mul_f32_e32 v1, 0x4f800000, v76
	v_cmp_gt_f32_e32 vcc, s3, v76
	s_nop 1
	v_cndmask_b32_e32 v1, v76, v1, vcc
	v_sqrt_f32_e32 v70, v1
	s_nop 0
	v_add_u32_e32 v6, -1, v70
	v_add_u32_e32 v7, 1, v70
	v_fma_f32 v8, -v6, v70, v1
	v_fma_f32 v9, -v7, v70, v1
	v_cmp_ge_f32_e64 s[4:5], 0, v8
	s_nop 1
	v_cndmask_b32_e64 v6, v70, v6, s[4:5]
	v_cmp_lt_f32_e64 s[4:5], 0, v9
	s_nop 1
	v_cndmask_b32_e64 v6, v6, v7, s[4:5]
	v_mul_f32_e32 v7, 0x37800000, v6
	v_cndmask_b32_e32 v6, v6, v7, vcc
	v_cmp_class_f32_e32 vcc, v1, v78
	s_nop 1
	v_cndmask_b32_e32 v1, v6, v1, vcc
	v_div_scale_f32 v6, s[4:5], v1, v1, 1.0
	v_rcp_f32_e32 v7, v6
	v_div_scale_f32 v4, vcc, 1.0, v1, 1.0
	v_fma_f32 v5, -v6, v7, 1.0
	v_fmac_f32_e32 v7, v5, v7
	v_mul_f32_e32 v5, v4, v7
	v_fma_f32 v8, -v6, v5, v4
	v_fmac_f32_e32 v5, v8, v7
	v_fma_f32 v4, -v6, v5, v4
	v_div_fmas_f32 v4, v4, v7, v5
	v_div_fixup_f32 v4, v4, v1, 1.0
	v_pk_mul_f32 v[6:7], v[54:55], v[4:5] op_sel_hi:[1,0]
	v_pk_mul_f32 v[8:9], v[56:57], v[4:5] op_sel_hi:[1,0]
	v_pk_mul_f32 v[10:11], v[58:59], v[4:5] op_sel_hi:[1,0]
	v_pk_mul_f32 v[12:13], v[60:61], v[4:5] op_sel_hi:[1,0]
	v_pk_mul_f32 v[14:15], v[62:63], v[4:5] op_sel_hi:[1,0]
	v_pk_mul_f32 v[16:17], v[64:65], v[4:5] op_sel_hi:[1,0]
	v_pk_mul_f32 v[18:19], v[66:67], v[4:5] op_sel_hi:[1,0]
	v_pk_mul_f32 v[4:5], v[68:69], v[4:5] op_sel_hi:[1,0]
	s_waitcnt vmcnt(10)
	v_pk_fma_f32 v[6:7], v[22:23], v[6:7], v[26:27]
	v_pk_fma_f32 v[8:9], v[24:25], v[8:9], v[28:29]
	s_waitcnt vmcnt(8)
	v_pk_fma_f32 v[10:11], v[30:31], v[10:11], v[34:35]
	v_pk_fma_f32 v[12:13], v[32:33], v[12:13], v[36:37]
	s_waitcnt vmcnt(6)
	v_pk_fma_f32 v[14:15], v[14:15], v[38:39], v[42:43]
	v_pk_fma_f32 v[16:17], v[16:17], v[40:41], v[44:45]
	s_waitcnt vmcnt(4)
	v_pk_fma_f32 v[18:19], v[18:19], v[46:47], v[50:51]
	v_pk_fma_f32 v[4:5], v[4:5], v[48:49], v[52:53]
	v_cvt_pk_f16_f32 v6, v6, v7
	v_cvt_pk_f16_f32 v7, v8, v9
	v_cvt_pk_f16_f32 v8, v10, v11
	v_cvt_pk_f16_f32 v9, v12, v13
	v_cvt_pk_f16_f32 v10, v14, v15
	v_cvt_pk_f16_f32 v11, v16, v17
	v_cvt_pk_f16_f32 v12, v18, v19
	v_cvt_pk_f16_f32 v13, v4, v5
	global_store_dwordx2 v[2:3], v[6:7], off
	global_store_dwordx2 v[2:3], v[8:9], off offset:512
	global_store_dwordx2 v[2:3], v[10:11], off offset:1024
	global_store_dwordx2 v[2:3], v[12:13], off offset:1536
	s_cbranch_execnz .LBB1_2

.LBB1_18:
	s_waitcnt lgkmcnt(0)
	s_mul_i32 s0, s10, s11
	s_abs_i32 s1, s0
	v_cvt_f32_u32_e32 v1, s1
	s_sub_i32 s16, 0, s1
	s_sub_i32 s2, s19, s2
	s_add_i32 s2, s2, s21
	v_rcp_iflag_f32_e32 v1, v1
	s_abs_i32 s11, s2
	s_xor_b32 s3, s2, s0
	s_ashr_i32 s3, s3, 31
	v_mul_f32_e32 v1, 0x4f7ffffe, v1
	v_cvt_u32_f32_e32 v1, v1
	v_lshrrev_b32_e32 v36, 4, v0
	v_lshlrev_b32_e32 v2, 4, v0
	v_and_b32_e32 v34, 0xf0, v2
	v_readfirstlane_b32 s17, v1
	s_mul_i32 s16, s16, s17
	s_mul_hi_u32 s16, s17, s16
	s_add_i32 s17, s17, s16
	s_mul_hi_u32 s16, s11, s17
	s_mul_i32 s17, s16, s1
	s_sub_i32 s11, s11, s17
	s_add_i32 s18, s16, 1
	s_sub_i32 s17, s11, s1
	s_cmp_ge_u32 s11, s1
	s_cselect_b32 s16, s18, s16
	s_cselect_b32 s11, s17, s11
	s_add_i32 s17, s16, 1
	s_cmp_ge_u32 s11, s1
	s_cselect_b32 s1, s17, s16
	s_abs_i32 s11, s10
	v_cvt_f32_u32_e32 v1, s11
	s_xor_b32 s1, s1, s3
	s_sub_i32 s16, 0, s11
	s_sub_i32 s3, s1, s3
	v_rcp_iflag_f32_e32 v1, v1
	s_mul_i32 s0, s3, s0
	s_sub_i32 s0, s2, s0
	s_abs_i32 s2, s0
	v_mul_f32_e32 v1, 0x4f7ffffe, v1
	v_cvt_u32_f32_e32 v1, v1
	s_xor_b32 s1, s0, s10
	s_ashr_i32 s1, s1, 31
	v_mov_b32_e32 v35, 0
	v_readfirstlane_b32 s17, v1
	s_mul_i32 s16, s16, s17
	s_mul_hi_u32 s16, s17, s16
	s_add_i32 s17, s17, s16
	s_mul_hi_u32 s16, s2, s17
	s_mul_i32 s17, s16, s11
	s_sub_i32 s2, s2, s17
	s_add_i32 s18, s16, 1
	s_sub_i32 s17, s2, s11
	s_cmp_ge_u32 s2, s11
	s_cselect_b32 s16, s18, s16
	s_cselect_b32 s2, s17, s2
	s_add_i32 s17, s16, 1
	s_cmp_ge_u32 s2, s11
	s_cselect_b32 s2, s17, s16
	s_xor_b32 s2, s2, s1
	s_sub_i32 s2, s2, s1
	s_mul_i32 s1, s2, s10
	s_ashr_i32 s11, s3, 31
	s_sub_i32 s10, s0, s1
	s_mul_i32 s0, s12, s11
	s_mul_hi_u32 s1, s12, s3
	s_add_i32 s0, s1, s0
	s_mul_i32 s1, s13, s3
	s_add_i32 s1, s0, s1
	s_mul_i32 s0, s12, s3
	s_lshl_b64 s[0:1], s[0:1], 2
	s_add_u32 s4, s4, s0
	s_addc_u32 s12, s5, s1
	s_mul_i32 s0, s14, s11
	s_mul_hi_u32 s1, s14, s3
	s_add_i32 s0, s1, s0
	s_mul_i32 s1, s15, s3
	s_add_i32 s5, s0, s1
	s_lshl_b32 s0, s10, 6
	s_ashr_i32 s1, s0, 31
	s_lshl_b32 s2, s2, 7
	s_lshl_b64 s[10:11], s[0:1], 2
	s_add_u32 s10, s4, s10
	v_or_b32_e32 v1, s2, v36
	s_addc_u32 s11, s12, s11
	v_lshl_add_u64 v[30:31], s[10:11], 0, v[34:35]
	v_mad_i64_i32 v[2:3], s[10:11], v1, s9, 0
	v_lshl_add_u64 v[10:11], v[2:3], 2, v[30:31]
	v_or_b32_e32 v2, 16, v1
	v_mad_i64_i32 v[2:3], s[10:11], v2, s9, 0
	v_lshl_add_u64 v[12:13], v[2:3], 2, v[30:31]
	global_load_dwordx4 v[2:5], v[10:11], off nt
	global_load_dwordx4 v[6:9], v[12:13], off nt
	v_or_b32_e32 v10, 32, v1
	v_mad_i64_i32 v[10:11], s[10:11], v10, s9, 0
	v_lshl_add_u64 v[18:19], v[10:11], 2, v[30:31]
	v_or_b32_e32 v10, 48, v1
	v_mad_i64_i32 v[10:11], s[10:11], v10, s9, 0
	v_lshl_add_u64 v[20:21], v[10:11], 2, v[30:31]
	global_load_dwordx4 v[10:13], v[18:19], off nt
	global_load_dwordx4 v[14:17], v[20:21], off nt
	v_or_b32_e32 v18, 64, v1
	v_mad_i64_i32 v[18:19], s[10:11], v18, s9, 0
	v_lshl_add_u64 v[26:27], v[18:19], 2, v[30:31]
	v_or_b32_e32 v18, 0x50, v1
	v_mad_i64_i32 v[18:19], s[10:11], v18, s9, 0
	v_lshl_add_u64 v[28:29], v[18:19], 2, v[30:31]
	global_load_dwordx4 v[18:21], v[26:27], off nt
	global_load_dwordx4 v[22:25], v[28:29], off nt
	v_or_b32_e32 v26, 0x60, v1
	v_mad_i64_i32 v[26:27], s[10:11], v26, s9, 0
	v_lshl_add_u64 v[26:27], v[26:27], 2, v[30:31]
	v_or_b32_e32 v1, 0x70, v1
	global_load_dwordx4 v[26:29], v[26:27], off nt
	v_mad_i64_i32 v[32:33], s[10:11], v1, s9, 0
	v_lshl_add_u64 v[30:31], v[32:33], 2, v[30:31]
	global_load_dwordx4 v[30:33], v[30:31], off nt
	s_movk_i32 s1, 0x104
	v_mad_u32_u24 v1, v36, s1, v34
	v_lshlrev_b32_e32 v0, 3, v0
	v_add_u32_e32 v34, 0x1040, v1
	v_add_u32_e32 v37, 0x1048, v1
	v_add_u32_e32 v38, 0x2080, v1
	v_add_u32_e32 v39, 0x2088, v1
	v_add_u32_e32 v40, 0x30c0, v1
	v_add_u32_e32 v41, 0x30c8, v1
	v_add_u32_e32 v42, 0x4100, v1
	v_add_u32_e32 v43, 0x4108, v1
	v_add_u32_e32 v44, 0x5140, v1
	v_and_b32_e32 v0, 0x78, v0
	s_mul_i32 s4, s14, s3
	s_lshl_b64 s[4:5], s[4:5], 1
	s_add_u32 s1, s6, s4
	s_addc_u32 s4, s7, s5
	s_ashr_i32 s3, s2, 31
	s_lshl_b64 s[2:3], s[2:3], 1
	s_add_u32 s2, s1, s2
	s_addc_u32 s3, s4, s3
	s_waitcnt vmcnt(7)
	ds_write2_b32 v1, v2, v3 offset1:1
	ds_write2_b32 v1, v4, v5 offset0:2 offset1:3
	s_waitcnt vmcnt(6)
	ds_write2_b32 v34, v6, v7 offset1:1
	ds_write2_b32 v37, v8, v9 offset1:1
	s_waitcnt vmcnt(5)
	ds_write2_b32 v38, v10, v11 offset1:1
	ds_write2_b32 v39, v12, v13 offset1:1
	s_waitcnt vmcnt(4)
	ds_write2_b32 v40, v14, v15 offset1:1
	ds_write2_b32 v41, v16, v17 offset1:1
	s_waitcnt vmcnt(3)
	ds_write2_b32 v42, v18, v19 offset1:1
	ds_write2_b32 v43, v20, v21 offset1:1
	s_waitcnt vmcnt(2)
	ds_write2_b32 v44, v22, v23 offset1:1
	v_add_u32_e32 v2, 0x5148, v1
	ds_write2_b32 v2, v24, v25 offset1:1
	v_add_u32_e32 v2, 0x6180, v1
	v_lshlrev_b32_e32 v34, 1, v0
	v_mul_u32_u24_e32 v0, 0x104, v0
	s_waitcnt vmcnt(1)
	ds_write2_b32 v2, v26, v27 offset1:1
	v_add_u32_e32 v2, 0x6188, v1
	v_lshl_add_u32 v24, v36, 2, v0
	ds_write2_b32 v2, v28, v29 offset1:1
	v_add_u32_e32 v2, 0x71c0, v1
	v_add_u32_e32 v1, 0x71c8, v1
	v_add_u32_e32 v25, 0x400, v24
	s_waitcnt vmcnt(0)
	ds_write2_b32 v2, v30, v31 offset1:1
	ds_write2_b32 v1, v32, v33 offset1:1
	s_waitcnt lgkmcnt(0)
	s_barrier
	ds_read2_b32 v[4:5], v24 offset1:16
	ds_read2_b32 v[6:7], v24 offset0:130 offset1:146
	ds_read2_b32 v[8:9], v25 offset0:4 offset1:20
	ds_read2_b32 v[10:11], v25 offset0:134 offset1:150
	ds_read2_b32 v[12:13], v25 offset0:199 offset1:215
	ds_read2_b32 v[14:15], v25 offset0:69 offset1:85
	ds_read2_b32 v[16:17], v24 offset0:195 offset1:211
	ds_read2_b32 v[18:19], v24 offset0:65 offset1:81
	v_or_b32_e32 v26, s0, v36
	v_lshl_add_u64 v[20:21], s[2:3], 0, v[34:35]
	v_mad_i64_i32 v[22:23], s[0:1], v26, s8, 0
	s_waitcnt lgkmcnt(3)
	v_cvt_pk_f16_f32 v3, v10, v12
	s_waitcnt lgkmcnt(2)
	v_cvt_pk_f16_f32 v2, v8, v14
	s_waitcnt lgkmcnt(1)
	v_cvt_pk_f16_f32 v1, v6, v16
	s_waitcnt lgkmcnt(0)
	v_cvt_pk_f16_f32 v0, v4, v18
	v_lshl_add_u64 v[22:23], v[22:23], 1, v[20:21]
	global_store_dwordx4 v[22:23], v[0:3], off
	v_or_b32_e32 v4, 16, v26
	s_nop 0
	v_cvt_pk_f16_f32 v3, v11, v13
	v_cvt_pk_f16_f32 v2, v9, v15
	v_cvt_pk_f16_f32 v1, v7, v17
	v_cvt_pk_f16_f32 v0, v5, v19
	ds_read2_b32 v[6:7], v24 offset0:32 offset1:48
	ds_read2_b32 v[8:9], v24 offset0:162 offset1:178
	ds_read2_b32 v[10:11], v25 offset0:36 offset1:52
	ds_read2_b32 v[12:13], v25 offset0:166 offset1:182
	ds_read2_b32 v[14:15], v25 offset0:231 offset1:247
	ds_read2_b32 v[16:17], v25 offset0:101 offset1:117
	ds_read2_b32 v[18:19], v24 offset0:227 offset1:243
	ds_read2_b32 v[22:23], v24 offset0:97 offset1:113
	v_mad_i64_i32 v[4:5], s[0:1], v4, s8, 0
	v_lshl_add_u64 v[4:5], v[4:5], 1, v[20:21]
	global_store_dwordx4 v[4:5], v[0:3], off
	v_or_b32_e32 v4, 32, v26
	v_mad_i64_i32 v[4:5], s[0:1], v4, s8, 0
	s_waitcnt lgkmcnt(3)
	v_cvt_pk_f16_f32 v3, v12, v14
	s_waitcnt lgkmcnt(2)
	v_cvt_pk_f16_f32 v2, v10, v16
	s_waitcnt lgkmcnt(1)
	v_cvt_pk_f16_f32 v1, v8, v18
	s_waitcnt lgkmcnt(0)
	v_cvt_pk_f16_f32 v0, v6, v22
	v_lshl_add_u64 v[4:5], v[4:5], 1, v[20:21]
	global_store_dwordx4 v[4:5], v[0:3], off
	v_or_b32_e32 v4, 48, v26
	v_mad_i64_i32 v[4:5], s[0:1], v4, s8, 0
	v_cvt_pk_f16_f32 v3, v13, v15
	v_cvt_pk_f16_f32 v2, v11, v17
	v_cvt_pk_f16_f32 v1, v9, v19
	v_cvt_pk_f16_f32 v0, v7, v23
	v_lshl_add_u64 v[4:5], v[4:5], 1, v[20:21]
	global_store_dwordx4 v[4:5], v[0:3], off
	s_endpgm
	s_endpgm
	s_endpgm
	s_endpgm
	s_endpgm
	s_endpgm
	s_endpgm
	s_endpgm
	s_endpgm
	s_endpgm
	s_endpgm
	s_endpgm
	s_endpgm
	s_endpgm
	s_endpgm
	s_endpgm
	s_endpgm
	s_endpgm
	s_endpgm
	s_endpgm
	s_endpgm
	s_endpgm
	s_endpgm
	s_endpgm
	s_endpgm
	s_endpgm
	s_endpgm
	s_endpgm
	s_endpgm
	s_endpgm
	s_endpgm
	s_endpgm
	s_endpgm
	s_endpgm
	s_endpgm
	s_endpgm
	s_endpgm
	s_endpgm
	s_endpgm
	s_endpgm
	s_endpgm
	s_endpgm
	s_endpgm
	s_endpgm
	.section	.rodata,"a",@progbits
	.p2align	6, 0x0

.Lat_nomask:
	v_max3_f32 v1, v44, v45, v46
	v_max3_f32 v26, v47, v48, v49
	v_max3_f32 v27, v50, v51, v52
	v_max3_f32 v1, v1, v53, v54
	v_max3_f32 v26, v26, v55, v56
	v_max3_f32 v27, v27, v57, v58
	v_max3_f32 v1, v1, v26, v27
	v_max_f32_e32 v1, v1, v59
	v_mov_b32_e32 v26, v1
	s_nop 1
	v_permlane16_swap_b32_e32 v1, v26
	v_max_f32_e32 v1, v1, v26
	v_mov_b32_e32 v26, v1
	s_nop 1
	v_permlane32_swap_b32_e32 v1, v26
	v_max3_f32 v1, v28, v1, v26
	v_sub_f32_e32 v26, v28, v1
	v_exp_f32_e32 v26, v26
	v_mov_b32_e32 v28, v1
	v_sub_f32_e32 v44, v44, v1
	v_sub_f32_e32 v45, v45, v1
	v_sub_f32_e32 v46, v46, v1
	v_sub_f32_e32 v47, v47, v1
	v_sub_f32_e32 v48, v48, v1
	v_sub_f32_e32 v49, v49, v1
	v_sub_f32_e32 v50, v50, v1
	v_sub_f32_e32 v51, v51, v1
	v_sub_f32_e32 v52, v52, v1
	v_sub_f32_e32 v53, v53, v1
	v_sub_f32_e32 v54, v54, v1
	v_sub_f32_e32 v55, v55, v1
	v_sub_f32_e32 v56, v56, v1
	v_sub_f32_e32 v57, v57, v1
	v_sub_f32_e32 v58, v58, v1
	v_sub_f32_e32 v59, v59, v1
	v_exp_f32_e32 v44, v44
	v_exp_f32_e32 v45, v45
	v_exp_f32_e32 v46, v46
	v_exp_f32_e32 v47, v47
	v_exp_f32_e32 v48, v48
	v_exp_f32_e32 v49, v49
	v_exp_f32_e32 v50, v50
	v_exp_f32_e32 v51, v51
	v_pk_mul_f32 v[100:101], v[26:27], v[100:101] op_sel_hi:[0,1]
	v_pk_mul_f32 v[102:103], v[26:27], v[102:103] op_sel_hi:[0,1]
	v_pk_mul_f32 v[104:105], v[26:27], v[104:105] op_sel_hi:[0,1]
	v_pk_mul_f32 v[106:107], v[26:27], v[106:107] op_sel_hi:[0,1]
	v_pk_mul_f32 v[108:109], v[26:27], v[108:109] op_sel_hi:[0,1]
	v_pk_mul_f32 v[110:111], v[26:27], v[110:111] op_sel_hi:[0,1]
	v_pk_mul_f32 v[112:113], v[26:27], v[112:113] op_sel_hi:[0,1]
	v_pk_mul_f32 v[114:115], v[26:27], v[114:115] op_sel_hi:[0,1]
	v_cvt_pk_f16_f32 v82, v44, v45
	v_cvt_pk_f16_f32 v83, v46, v47
	v_cvt_pk_f16_f32 v84, v48, v49
	v_cvt_pk_f16_f32 v85, v50, v51
	v_exp_f32_e32 v52, v52
	v_exp_f32_e32 v53, v53
	v_exp_f32_e32 v54, v54
	v_exp_f32_e32 v55, v55
	v_exp_f32_e32 v56, v56
	v_exp_f32_e32 v57, v57
	v_exp_f32_e32 v58, v58
	v_exp_f32_e32 v59, v59
	s_waitcnt lgkmcnt(0)
	v_mfma_f32_16x16x32_f16 v[100:103], v[86:89], v[82:85], v[100:103]
	ds_read_b64_tr_b16 v[86:87], v0 offset:17408
	ds_read_b64_tr_b16 v[88:89], v0 offset:17920
	v_mfma_f32_16x16x32_f16 v[104:107], v[90:93], v[82:85], v[104:107]
	ds_read_b64_tr_b16 v[90:91], v0 offset:19488
	ds_read_b64_tr_b16 v[92:93], v0 offset:20000
	v_mfma_f32_16x16x32_f16 v[108:111], v[94:97], v[82:85], v[108:111]
	ds_read_b64_tr_b16 v[94:95], v0 offset:21568
	ds_read_b64_tr_b16 v[96:97], v0 offset:22080
	v_mfma_f32_16x16x32_f16 v[112:115], v[14:17], v[82:85], v[112:115]
	ds_read_b64_tr_b16 v[14:15], v0 offset:23648
	ds_read_b64_tr_b16 v[16:17], v0 offset:24160
	v_cvt_pk_f16_f32 v78, v52, v53
	v_cvt_pk_f16_f32 v79, v54, v55
	v_cvt_pk_f16_f32 v80, v56, v57
	v_cvt_pk_f16_f32 v81, v58, v59
	v_pk_add_f32 v[18:19], v[44:45], v[46:47]
	v_pk_add_f32 v[20:21], v[48:49], v[50:51]
	v_pk_add_f32 v[22:23], v[52:53], v[54:55]
	v_pk_add_f32 v[24:25], v[56:57], v[58:59]
	v_pk_add_f32 v[18:19], v[18:19], v[20:21]
	v_pk_add_f32 v[22:23], v[22:23], v[24:25]
	s_waitcnt lgkmcnt(6)
	v_mfma_f32_16x16x32_f16 v[100:103], v[86:89], v[78:81], v[100:103]
	s_waitcnt lgkmcnt(4)
	v_mfma_f32_16x16x32_f16 v[104:107], v[90:93], v[78:81], v[104:107]
	s_waitcnt lgkmcnt(2)
	v_mfma_f32_16x16x32_f16 v[108:111], v[94:97], v[78:81], v[108:111]
	s_waitcnt lgkmcnt(0)
	v_mfma_f32_16x16x32_f16 v[112:115], v[14:17], v[78:81], v[112:115]
	v_pk_add_f32 v[18:19], v[18:19], v[22:23]
	s_cmp_lt_u32 s16, s3
	s_cbranch_scc0 .Lat_nowr
	s_xor_b32 s12, s17, 1
	s_mul_i32 s13, s12, 0x2080
	s_lshl_b32 s12, s12, 13
	v_add_u32_e32 v1, s12, v34
	v_add_u32_e32 v60, s13, v37
	s_waitcnt vmcnt(0)
	ds_write_b128 v1, v[62:65]
	ds_write_b128 v1, v[66:69] offset:4096
	ds_write_b128 v60, v[70:73] offset:16384
	ds_write_b128 v60, v[74:77] offset:17408

.LBB3_14:
	s_endpgm
	s_endpgm
	s_endpgm
	s_endpgm
	s_endpgm
	s_endpgm
	s_endpgm
	s_endpgm
	s_endpgm
	s_endpgm
	s_endpgm
	s_endpgm
	s_endpgm
	s_endpgm
	s_endpgm
	s_endpgm
	s_endpgm
	s_endpgm
	.section	.rodata,"a",@progbits
	.p2align	6, 0x0

_Z9ln_kernelILi2EEvPKiPKfS3_PfS3_S3_PDF16_:
	s_load_dwordx8 s[4:11], s[0:1], 0x8
	v_and_b32_e32 v12, 63, v0
	v_lshrrev_b32_e32 v0, 6, v0
	v_lshl_or_b32 v6, s2, 2, v0
	v_ashrrev_i32_e32 v7, 31, v6
	v_lshlrev_b64 v[2:3], 11, v[6:7]
	v_mov_b32_e32 v1, 0
	s_waitcnt lgkmcnt(0)
	v_lshl_add_u64 v[8:9], s[4:5], 0, v[2:3]
	v_lshlrev_b32_e32 v4, 3, v12
	v_mov_b32_e32 v5, v1
	v_lshl_add_u64 v[8:9], v[8:9], 0, v[4:5]
	s_mov_b64 s[2:3], 0x400000
	v_lshl_add_u64 v[10:11], v[8:9], 0, s[2:3]
	s_mov_b32 s2, 0x400000
	global_load_dwordx2 v[16:17], v[8:9], off
	global_load_dwordx2 v[18:19], v[8:9], off offset:512
	global_load_dwordx2 v[20:21], v[8:9], off offset:1024
	global_load_dwordx2 v[22:23], v[8:9], off offset:1536
	v_add_co_u32_e32 v8, vcc, s2, v8
	global_load_dwordx2 v[24:25], v[10:11], off offset:512
	global_load_dwordx2 v[26:27], v[10:11], off offset:1024
	global_load_dwordx2 v[28:29], v[10:11], off offset:1536
	v_addc_co_u32_e32 v9, vcc, 0, v9, vcc
	global_load_dwordx2 v[30:31], v[8:9], off
	v_lshlrev_b64 v[6:7], 12, v[6:7]
	v_lshlrev_b32_e32 v0, 4, v12
	v_lshl_add_u64 v[6:7], s[8:9], 0, v[6:7]
	v_lshl_add_u64 v[6:7], v[6:7], 0, v[0:1]
	global_load_dwordx4 v[8:11], v[6:7], off offset:1024
	global_load_dwordx4 v[12:15], v0, s[6:7] offset:1024
	s_waitcnt vmcnt(9)
	v_cvt_f32_f16_e32 v32, v16
	s_waitcnt vmcnt(8)
	v_cvt_f32_f16_e32 v36, v18
	v_cvt_f32_f16_sdwa v37, v18 dst_sel:DWORD dst_unused:UNUSED_PAD src0_sel:WORD_1
	v_cvt_f32_f16_e32 v38, v19
	v_cvt_f32_f16_sdwa v39, v19 dst_sel:DWORD dst_unused:UNUSED_PAD src0_sel:WORD_1
	s_waitcnt vmcnt(7)
	v_cvt_f32_f16_e32 v40, v20
	v_cvt_f32_f16_sdwa v41, v20 dst_sel:DWORD dst_unused:UNUSED_PAD src0_sel:WORD_1
	v_cvt_f32_f16_e32 v42, v21
	v_cvt_f32_f16_sdwa v43, v21 dst_sel:DWORD dst_unused:UNUSED_PAD src0_sel:WORD_1
	s_waitcnt vmcnt(6)
	v_cvt_f32_f16_e32 v44, v22
	v_cvt_f32_f16_sdwa v45, v22 dst_sel:DWORD dst_unused:UNUSED_PAD src0_sel:WORD_1
	v_cvt_f32_f16_e32 v46, v23
	v_cvt_f32_f16_sdwa v47, v23 dst_sel:DWORD dst_unused:UNUSED_PAD src0_sel:WORD_1
	s_waitcnt vmcnt(5)
	v_cvt_f32_f16_e32 v20, v24
	v_cvt_f32_f16_sdwa v21, v24 dst_sel:DWORD dst_unused:UNUSED_PAD src0_sel:WORD_1
	v_cvt_f32_f16_e32 v22, v25
	v_cvt_f32_f16_sdwa v23, v25 dst_sel:DWORD dst_unused:UNUSED_PAD src0_sel:WORD_1
	s_waitcnt vmcnt(4)
	v_cvt_f32_f16_e32 v24, v26
	v_cvt_f32_f16_sdwa v25, v26 dst_sel:DWORD dst_unused:UNUSED_PAD src0_sel:WORD_1
	v_cvt_f32_f16_e32 v26, v27
	v_cvt_f32_f16_sdwa v27, v27 dst_sel:DWORD dst_unused:UNUSED_PAD src0_sel:WORD_1
	s_waitcnt vmcnt(3)
	v_cvt_f32_f16_e32 v48, v28
	v_cvt_f32_f16_sdwa v49, v28 dst_sel:DWORD dst_unused:UNUSED_PAD src0_sel:WORD_1
	v_cvt_f32_f16_e32 v28, v29
	v_cvt_f32_f16_sdwa v29, v29 dst_sel:DWORD dst_unused:UNUSED_PAD src0_sel:WORD_1
	v_cvt_f32_f16_sdwa v33, v16 dst_sel:DWORD dst_unused:UNUSED_PAD src0_sel:WORD_1
	v_cvt_f32_f16_e32 v34, v17
	v_cvt_f32_f16_sdwa v35, v17 dst_sel:DWORD dst_unused:UNUSED_PAD src0_sel:WORD_1
	s_waitcnt vmcnt(2)
	v_cvt_f32_f16_e32 v50, v30
	v_cvt_f32_f16_sdwa v51, v30 dst_sel:DWORD dst_unused:UNUSED_PAD src0_sel:WORD_1
	v_cvt_f32_f16_e32 v52, v31
	v_cvt_f32_f16_sdwa v53, v31 dst_sel:DWORD dst_unused:UNUSED_PAD src0_sel:WORD_1
	global_load_dwordx4 v[16:19], v[6:7], off
	v_pk_add_f32 v[36:37], v[36:37], v[20:21]
	v_pk_add_f32 v[38:39], v[38:39], v[22:23]
	global_load_dwordx4 v[20:23], v[6:7], off offset:2048
	v_pk_add_f32 v[40:41], v[40:41], v[24:25]
	v_pk_add_f32 v[42:43], v[42:43], v[26:27]
	global_load_dwordx4 v[24:27], v[6:7], off offset:3072
	v_pk_add_f32 v[46:47], v[46:47], v[28:29]
	global_load_dwordx4 v[28:31], v0, s[6:7] offset:2048
	s_waitcnt vmcnt(5)
	v_pk_add_f32 v[36:37], v[8:9], v[36:37]
	v_pk_add_f32 v[38:39], v[10:11], v[38:39]
	global_load_dwordx4 v[8:11], v0, s[6:7]
	v_pk_add_f32 v[44:45], v[44:45], v[48:49]
	v_pk_add_f32 v[48:49], v[32:33], v[50:51]
	v_pk_add_f32 v[50:51], v[34:35], v[52:53]
	global_load_dwordx4 v[32:35], v0, s[6:7] offset:3072
	s_waitcnt vmcnt(6)
	v_pk_add_f32 v[12:13], v[12:13], v[36:37]
	v_pk_add_f32 v[14:15], v[14:15], v[38:39]
	s_load_dwordx4 s[4:7], s[0:1], 0x28
	s_mov_b32 s0, 0xf800000
	s_waitcnt lgkmcnt(0)
	v_lshl_add_u64 v[2:3], s[6:7], 0, v[2:3]
	s_waitcnt vmcnt(4)
	v_pk_add_f32 v[20:21], v[20:21], v[40:41]
	v_pk_add_f32 v[22:23], v[22:23], v[42:43]
	v_pk_add_f32 v[40:41], v[16:17], v[48:49]
	v_pk_add_f32 v[42:43], v[18:19], v[50:51]
	s_waitcnt vmcnt(3)
	v_pk_add_f32 v[24:25], v[24:25], v[44:45]
	v_pk_add_f32 v[26:27], v[26:27], v[46:47]
	s_waitcnt vmcnt(2)
	v_pk_add_f32 v[16:17], v[28:29], v[20:21]
	v_pk_add_f32 v[18:19], v[30:31], v[22:23]
	s_waitcnt vmcnt(1)
	v_pk_add_f32 v[8:9], v[8:9], v[40:41]
	v_pk_add_f32 v[10:11], v[10:11], v[42:43]
	v_mov_b32_e32 v28, v13
	v_mov_b32_e32 v29, v15
	s_waitcnt vmcnt(0)
	v_pk_add_f32 v[20:21], v[32:33], v[24:25]
	v_pk_add_f32 v[22:23], v[34:35], v[26:27]
	v_mov_b32_e32 v24, v8
	v_mov_b32_e32 v25, v10
	v_mov_b32_e32 v26, v9
	v_mov_b32_e32 v27, v11
	v_pk_add_f32 v[24:25], v[24:25], v[26:27]
	v_mov_b32_e32 v26, v12
	v_mov_b32_e32 v27, v14
	v_pk_add_f32 v[26:27], v[26:27], v[28:29]
	v_add_f32_e32 v1, v24, v25
	v_pk_add_f32 v[26:27], v[26:27], v[26:27] op_sel:[0,1] op_sel_hi:[1,0]
	v_pk_add_f32 v[28:29], v[16:17], v[16:17] op_sel:[0,1] op_sel_hi:[1,0]
	v_pk_add_f32 v[30:31], v[18:19], v[18:19] op_sel:[0,1] op_sel_hi:[1,0]
	v_add_f32_e32 v24, 0, v1
	v_mov_b32_e32 v25, v20
	v_mov_b32_e32 v27, v21
	v_mov_b32_e32 v29, v22
	v_mov_b32_e32 v31, v23
	v_pk_add_f32 v[24:25], v[24:25], v[26:27]
	v_pk_add_f32 v[26:27], v[28:29], v[30:31]
	s_nop 0
	v_pk_add_f32 v[24:25], v[24:25], v[26:27]
	s_nop 0
	v_add_f32_e32 v1, v24, v25
	v_mbcnt_lo_u32_b32 v24, -1, 0
	v_mbcnt_hi_u32_b32 v24, -1, v24
	v_and_b32_e32 v25, 64, v24
	v_add_u32_e32 v25, 64, v25
	v_xor_b32_e32 v26, 32, v24
	v_cmp_lt_i32_e32 vcc, v26, v25
	s_nop 1
	v_cndmask_b32_e32 v26, v24, v26, vcc
	v_lshlrev_b32_e32 v52, 2, v26
	v_mov_b32_e32 v26, v1
	s_waitcnt lgkmcnt(0)
	s_nop 1
	v_permlane32_swap_b32_e32 v1, v26
	v_add_f32_e32 v1, v1, v26
	v_xor_b32_e32 v26, 16, v24
	v_cmp_lt_i32_e32 vcc, v26, v25
	s_nop 1
	v_cndmask_b32_e32 v26, v24, v26, vcc
	v_lshlrev_b32_e32 v53, 2, v26
	v_mov_b32_e32 v26, v1
	s_waitcnt lgkmcnt(0)
	s_nop 1
	v_permlane16_swap_b32_e32 v1, v26
	v_add_f32_e32 v1, v1, v26
	v_xor_b32_e32 v26, 8, v24
	v_cmp_lt_i32_e32 vcc, v26, v25
	s_nop 1
	v_cndmask_b32_e32 v26, v24, v26, vcc
	v_lshlrev_b32_e32 v54, 2, v26
	s_waitcnt lgkmcnt(0)
	s_nop 1
	v_add_f32_dpp v1, v1, v1 row_ror:8 row_mask:0xf bank_mask:0xf
	v_xor_b32_e32 v26, 4, v24
	v_cmp_lt_i32_e32 vcc, v26, v25
	s_nop 1
	v_cndmask_b32_e32 v26, v24, v26, vcc
	v_lshlrev_b32_e32 v55, 2, v26
	s_waitcnt lgkmcnt(0)
	s_nop 1
	v_add_f32_dpp v1, v1, v1 row_ror:4 row_mask:0xf bank_mask:0xf
	v_xor_b32_e32 v26, 2, v24
	v_cmp_lt_i32_e32 vcc, v26, v25
	s_nop 1
	v_cndmask_b32_e32 v26, v24, v26, vcc
	v_lshlrev_b32_e32 v56, 2, v26
	s_waitcnt lgkmcnt(0)
	s_nop 1
	v_add_f32_dpp v1, v1, v1 row_ror:2 row_mask:0xf bank_mask:0xf
	v_xor_b32_e32 v26, 1, v24
	v_cmp_lt_i32_e32 vcc, v26, v25
	s_nop 1
	v_cndmask_b32_e32 v24, v24, v26, vcc
	v_lshlrev_b32_e32 v57, 2, v24
	s_waitcnt lgkmcnt(0)
	s_nop 1
	v_add_f32_dpp v1, v1, v1 row_ror:1 row_mask:0xf bank_mask:0xf
	v_mul_f32_e32 v24, 0x3a800000, v1
	v_pk_add_f32 v[36:37], v[8:9], v[24:25] op_sel_hi:[1,0] neg_lo:[0,1] neg_hi:[0,1]
	v_pk_add_f32 v[38:39], v[10:11], v[24:25] op_sel_hi:[1,0] neg_lo:[0,1] neg_hi:[0,1]
	v_mov_b32_e32 v28, v37
	v_mov_b32_e32 v29, v39
	v_pk_add_f32 v[40:41], v[12:13], v[24:25] op_sel_hi:[1,0] neg_lo:[0,1] neg_hi:[0,1]
	v_pk_add_f32 v[42:43], v[14:15], v[24:25] op_sel_hi:[1,0] neg_lo:[0,1] neg_hi:[0,1]
	v_mov_b32_e32 v26, v36
	v_mov_b32_e32 v27, v38
	v_pk_mul_f32 v[28:29], v[28:29], v[28:29]
	v_mov_b32_e32 v30, v41
	v_mov_b32_e32 v31, v43
	v_pk_fma_f32 v[26:27], v[26:27], v[26:27], v[28:29]
	v_mov_b32_e32 v28, v40
	v_mov_b32_e32 v29, v42
	v_pk_mul_f32 v[30:31], v[30:31], v[30:31]
	v_pk_add_f32 v[44:45], v[16:17], v[24:25] op_sel_hi:[1,0] neg_lo:[0,1] neg_hi:[0,1]
	v_pk_fma_f32 v[28:29], v[28:29], v[28:29], v[30:31]
	v_mul_f32_e32 v30, v44, v44
	v_pk_fma_f32 v[30:31], v[44:45], v[44:45], v[30:31] op_sel_hi:[1,1,0]
	v_pk_add_f32 v[46:47], v[18:19], v[24:25] op_sel_hi:[1,0] neg_lo:[0,1] neg_hi:[0,1]
	v_pk_add_f32 v[48:49], v[20:21], v[24:25] op_sel_hi:[1,0] neg_lo:[0,1] neg_hi:[0,1]
	v_mul_f32_e32 v30, v46, v46
	v_pk_add_f32 v[50:51], v[22:23], v[24:25] op_sel_hi:[1,0] neg_lo:[0,1] neg_hi:[0,1]
	v_pk_fma_f32 v[32:33], v[46:47], v[46:47], v[30:31] op_sel_hi:[1,1,0]
	v_pk_mul_f32 v[34:35], v[48:49], v[48:49]
	v_pk_add_f32 v[26:27], v[26:27], v[26:27] op_sel_hi:[0,1]
	v_pk_add_f32 v[28:29], v[28:29], v[28:29] op_sel_hi:[0,1]
	v_pk_mul_f32 v[24:25], v[50:51], v[50:51]
	v_mov_b32_e32 v30, v34
	v_mov_b32_e32 v32, v35
	v_mov_b32_e32 v26, v24
	v_mov_b32_e32 v28, v25
	v_pk_add_f32 v[30:31], v[30:31], v[32:33]
	v_pk_add_f32 v[24:25], v[26:27], v[28:29]
	s_nop 0
	v_pk_add_f32 v[24:25], v[30:31], v[24:25]
	s_nop 0
	v_add_f32_e32 v1, v24, v25
	v_mov_b32_e32 v24, v1
	s_waitcnt lgkmcnt(0)
	s_nop 1
	v_permlane32_swap_b32_e32 v1, v24
	v_add_f32_e32 v1, v1, v24
	v_mov_b32_e32 v24, v1
	s_waitcnt lgkmcnt(0)
	s_nop 1
	v_permlane16_swap_b32_e32 v1, v24
	v_add_f32_e32 v1, v1, v24
	s_waitcnt lgkmcnt(0)
	s_nop 1
	v_add_f32_dpp v1, v1, v1 row_ror:8 row_mask:0xf bank_mask:0xf
	s_waitcnt lgkmcnt(0)
	s_nop 1
	v_add_f32_dpp v1, v1, v1 row_ror:4 row_mask:0xf bank_mask:0xf
	global_load_dwordx4 v[24:27], v0, s[10:11]
	global_load_dwordx4 v[28:31], v0, s[10:11] offset:1024
	s_waitcnt lgkmcnt(0)
	s_nop 1
	v_add_f32_dpp v1, v1, v1 row_ror:2 row_mask:0xf bank_mask:0xf
	global_store_dwordx4 v[6:7], v[8:11], off
	global_store_dwordx4 v[6:7], v[12:15], off offset:1024
	global_store_dwordx4 v[6:7], v[16:19], off offset:2048
	global_store_dwordx4 v[6:7], v[20:23], off offset:3072
	s_waitcnt lgkmcnt(0)
	s_nop 1
	v_add_f32_dpp v1, v1, v1 row_ror:1 row_mask:0xf bank_mask:0xf
	v_mov_b32_e32 v32, 0x3727c5ac
	v_fmac_f32_e32 v32, 0x3a800000, v1
	v_mul_f32_e32 v1, 0x4f800000, v32
	v_cmp_gt_f32_e32 vcc, s0, v32
	global_load_dwordx4 v[12:15], v0, s[4:5]
	global_load_dwordx4 v[16:19], v0, s[4:5] offset:1024
	v_cndmask_b32_e32 v1, v32, v1, vcc
	v_sqrt_f32_e32 v32, v1
	global_load_dwordx4 v[8:11], v0, s[10:11] offset:2048
	v_add_u32_e32 v6, -1, v32
	v_fma_f32 v7, -v6, v32, v1
	v_cmp_ge_f32_e64 s[0:1], 0, v7
	v_add_u32_e32 v7, 1, v32
	v_fma_f32 v20, -v7, v32, v1
	v_cndmask_b32_e64 v6, v32, v6, s[0:1]
	v_cmp_lt_f32_e64 s[0:1], 0, v20
	global_load_dwordx4 v[20:23], v0, s[4:5] offset:2048
	s_nop 0
	v_cndmask_b32_e64 v6, v6, v7, s[0:1]
	v_mul_f32_e32 v7, 0x37800000, v6
	v_cndmask_b32_e32 v6, v6, v7, vcc
	v_mov_b32_e32 v7, 0x260
	v_cmp_class_f32_e32 vcc, v1, v7
	s_nop 1
	v_cndmask_b32_e32 v1, v6, v1, vcc
	v_div_scale_f32 v32, s[0:1], v1, v1, 1.0
	v_rcp_f32_e32 v33, v32
	v_lshl_add_u64 v[6:7], v[2:3], 0, v[4:5]
	v_div_scale_f32 v34, vcc, 1.0, v1, 1.0
	v_fma_f32 v2, -v32, v33, 1.0
	v_fmac_f32_e32 v33, v2, v33
	v_mul_f32_e32 v35, v34, v33
	v_fma_f32 v2, -v32, v35, v34
	v_fmac_f32_e32 v35, v2, v33
	v_fma_f32 v32, -v32, v35, v34
	global_load_dwordx4 v[2:5], v0, s[10:11] offset:3072
	v_div_fmas_f32 v52, v32, v33, v35
	global_load_dwordx4 v[32:35], v0, s[4:5] offset:3072
	v_div_fixup_f32 v0, v52, v1, 1.0
	v_pk_mul_f32 v[36:37], v[36:37], v[0:1] op_sel_hi:[1,0]
	s_waitcnt vmcnt(5)
	v_pk_fma_f32 v[12:13], v[24:25], v[36:37], v[12:13]
	v_pk_mul_f32 v[24:25], v[38:39], v[0:1] op_sel_hi:[1,0]
	v_cvt_pk_f16_f32 v12, v12, v13
	v_pk_fma_f32 v[14:15], v[26:27], v[24:25], v[14:15]
	s_nop 0
	v_cvt_pk_f16_f32 v13, v14, v15
	global_store_dwordx2 v[6:7], v[12:13], off
	v_pk_mul_f32 v[12:13], v[40:41], v[0:1] op_sel_hi:[1,0]
	v_pk_mul_f32 v[14:15], v[42:43], v[0:1] op_sel_hi:[1,0]
	s_waitcnt vmcnt(5)
	v_pk_fma_f32 v[12:13], v[28:29], v[12:13], v[16:17]
	v_pk_fma_f32 v[14:15], v[30:31], v[14:15], v[18:19]
	v_cvt_pk_f16_f32 v12, v12, v13
	v_cvt_pk_f16_f32 v13, v14, v15
	global_store_dwordx2 v[6:7], v[12:13], off offset:512
	v_pk_mul_f32 v[12:13], v[44:45], v[0:1] op_sel_hi:[1,0]
	s_waitcnt vmcnt(4)
	v_pk_fma_f32 v[8:9], v[12:13], v[8:9], v[20:21]
	v_pk_mul_f32 v[12:13], v[46:47], v[0:1] op_sel_hi:[1,0]
	v_cvt_pk_f16_f32 v8, v8, v9
	v_pk_fma_f32 v[10:11], v[12:13], v[10:11], v[22:23]
	s_nop 0
	v_cvt_pk_f16_f32 v9, v10, v11
	global_store_dwordx2 v[6:7], v[8:9], off offset:1024
	v_pk_mul_f32 v[8:9], v[48:49], v[0:1] op_sel_hi:[1,0]
	v_pk_mul_f32 v[0:1], v[50:51], v[0:1] op_sel_hi:[1,0]
	s_waitcnt vmcnt(3)
	v_pk_fma_f32 v[2:3], v[8:9], v[2:3], v[32:33]
	v_pk_fma_f32 v[0:1], v[0:1], v[4:5], v[34:35]
	v_cvt_pk_f16_f32 v2, v2, v3
	v_cvt_pk_f16_f32 v3, v0, v1
	global_store_dwordx2 v[6:7], v[2:3], off offset:1536
	s_endpgm
	s_endpgm
	s_endpgm
	s_endpgm
	s_endpgm
	s_endpgm
	s_endpgm
	s_endpgm
	s_endpgm
	s_endpgm

_Z9ln_kernelILi0EEvPKiPKfS3_PfS3_S3_PDF16_:
	s_load_dwordx8 s[4:11], s[0:1], 0x18
	v_and_b32_e32 v52, 63, v0
	v_lshrrev_b32_e32 v0, 6, v0
	v_lshl_or_b32 v0, s2, 2, v0
	v_ashrrev_i32_e32 v1, 31, v0
	v_lshlrev_b64 v[2:3], 12, v[0:1]
	s_waitcnt lgkmcnt(0)
	v_lshl_add_u64 v[4:5], s[4:5], 0, v[2:3]
	v_lshlrev_b32_e32 v2, 4, v52
	v_mov_b32_e32 v3, 0
	v_lshl_add_u64 v[20:21], v[4:5], 0, v[2:3]
	global_load_dwordx4 v[4:7], v[20:21], off offset:1024
	global_load_dwordx4 v[8:11], v[20:21], off offset:2048
	global_load_dwordx4 v[12:15], v[20:21], off
	global_load_dwordx4 v[16:19], v[20:21], off offset:3072
	v_mbcnt_lo_u32_b32 v20, -1, 0
	v_mbcnt_hi_u32_b32 v32, -1, v20
	v_and_b32_e32 v20, 64, v32
	v_xor_b32_e32 v21, 32, v32
	v_add_u32_e32 v34, 64, v20
	v_cmp_lt_i32_e32 vcc, v21, v34
	v_xor_b32_e32 v33, 16, v32
	s_mov_b32 s0, 0xf800000
	v_cndmask_b32_e32 v20, v32, v21, vcc
	v_lshlrev_b32_e32 v53, 2, v20
	v_cmp_lt_i32_e32 vcc, v33, v34
	v_lshlrev_b64 v[0:1], 11, v[0:1]
	v_lshl_add_u64 v[0:1], s[10:11], 0, v[0:1]
	s_waitcnt vmcnt(3)
	v_mov_b32_e32 v36, v5
	v_mov_b32_e32 v37, v6
	v_mov_b32_e32 v5, v7
	s_waitcnt vmcnt(1)
	v_mov_b32_e32 v22, v12
	v_mov_b32_e32 v23, v14
	v_mov_b32_e32 v24, v13
	v_mov_b32_e32 v25, v15
	v_mov_b32_e32 v6, v9
	v_mov_b32_e32 v20, v11
	s_waitcnt vmcnt(0)
	v_mov_b32_e32 v21, v16
	v_pk_add_f32 v[26:27], v[36:37], v[4:5]
	v_pk_add_f32 v[22:23], v[22:23], v[24:25]
	v_pk_add_f32 v[28:29], v[8:9], v[6:7]
	v_pk_add_f32 v[30:31], v[10:11], v[20:21]
	v_pk_add_f32 v[24:25], v[26:27], v[26:27] op_sel:[0,1] op_sel_hi:[1,0]
	v_add_f32_e32 v5, v22, v23
	v_mov_b32_e32 v29, v18
	v_mov_b32_e32 v31, v19
	v_add_f32_e32 v20, 0, v5
	v_mov_b32_e32 v25, v17
	v_pk_add_f32 v[22:23], v[28:29], v[30:31]
	v_pk_add_f32 v[20:21], v[20:21], v[24:25]
	v_pk_mov_b32 v[36:37], v[36:37], v[36:37] op_sel:[1,0]
	v_pk_add_f32 v[20:21], v[20:21], v[22:23]
	s_nop 0
	v_add_f32_e32 v5, v20, v21
	v_mov_b32_e32 v6, v5
	v_cndmask_b32_e32 v21, v32, v33, vcc
	v_lshlrev_b32_e32 v54, 2, v21
	v_xor_b32_e32 v20, 8, v32
	v_cmp_lt_i32_e32 vcc, v20, v34
	s_waitcnt lgkmcnt(0)
	s_nop 1
	v_permlane32_swap_b32_e32 v5, v6
	v_add_f32_e32 v5, v5, v6
	v_mov_b32_e32 v6, v5
	v_cndmask_b32_e32 v20, v32, v20, vcc
	v_lshlrev_b32_e32 v55, 2, v20
	v_xor_b32_e32 v21, 4, v32
	v_cmp_lt_i32_e32 vcc, v21, v34
	s_waitcnt lgkmcnt(0)
	s_nop 1
	v_permlane16_swap_b32_e32 v5, v6
	v_add_f32_e32 v5, v5, v6
	v_cndmask_b32_e32 v21, v32, v21, vcc
	v_lshlrev_b32_e32 v56, 2, v21
	v_xor_b32_e32 v20, 2, v32
	v_cmp_lt_i32_e32 vcc, v20, v34
	s_waitcnt lgkmcnt(0)
	s_nop 1
	v_add_f32_dpp v5, v5, v5 row_ror:8 row_mask:0xf bank_mask:0xf
	v_cndmask_b32_e32 v20, v32, v20, vcc
	v_lshlrev_b32_e32 v57, 2, v20
	v_xor_b32_e32 v21, 1, v32
	v_cmp_lt_i32_e32 vcc, v21, v34
	s_waitcnt lgkmcnt(0)
	s_nop 1
	v_add_f32_dpp v5, v5, v5 row_ror:4 row_mask:0xf bank_mask:0xf
	v_cndmask_b32_e32 v20, v32, v21, vcc
	v_lshlrev_b32_e32 v58, 2, v20
	global_load_dwordx4 v[20:23], v2, s[6:7]
	global_load_dwordx4 v[24:27], v2, s[8:9]
	global_load_dwordx4 v[28:31], v2, s[6:7] offset:1024
	global_load_dwordx4 v[32:35], v2, s[8:9] offset:1024
	s_waitcnt lgkmcnt(0)
	s_nop 1
	v_add_f32_dpp v6, v5, v5 row_ror:2 row_mask:0xf bank_mask:0xf
	v_mov_b32_e32 v5, v37
	v_mov_b32_e32 v37, v7
	s_waitcnt lgkmcnt(0)
	s_nop 1
	v_add_f32_dpp v6, v6, v6 row_ror:1 row_mask:0xf bank_mask:0xf
	v_mul_f32_e32 v6, 0x3a800000, v6
	v_pk_add_f32 v[38:39], v[12:13], v[6:7] op_sel_hi:[1,0] neg_lo:[0,1] neg_hi:[0,1]
	v_pk_add_f32 v[40:41], v[14:15], v[6:7] op_sel_hi:[1,0] neg_lo:[0,1] neg_hi:[0,1]
	v_pk_add_f32 v[46:47], v[4:5], v[6:7] op_sel_hi:[1,0] neg_lo:[0,1] neg_hi:[0,1]
	v_pk_add_f32 v[36:37], v[36:37], v[6:7] op_sel_hi:[1,0] neg_lo:[0,1] neg_hi:[0,1]
	v_pk_add_f32 v[42:43], v[16:17], v[6:7] op_sel_hi:[1,0] neg_lo:[0,1] neg_hi:[0,1]
	v_pk_add_f32 v[44:45], v[18:19], v[6:7] op_sel_hi:[1,0] neg_lo:[0,1] neg_hi:[0,1]
	v_pk_add_f32 v[48:49], v[8:9], v[6:7] op_sel_hi:[1,0] neg_lo:[0,1] neg_hi:[0,1]
	v_pk_add_f32 v[50:51], v[10:11], v[6:7] op_sel_hi:[1,0] neg_lo:[0,1] neg_hi:[0,1]
	v_mov_b32_e32 v6, v39
	v_mov_b32_e32 v7, v41
	v_mov_b32_e32 v14, v47
	v_mov_b32_e32 v15, v37
	v_mov_b32_e32 v4, v38
	v_mov_b32_e32 v5, v40
	v_mov_b32_e32 v12, v46
	v_mov_b32_e32 v13, v36
	v_pk_mul_f32 v[6:7], v[6:7], v[6:7]
	v_pk_mul_f32 v[14:15], v[14:15], v[14:15]
	v_mul_f32_e32 v16, v48, v48
	v_mul_f32_e32 v18, v50, v50
	v_pk_fma_f32 v[4:5], v[4:5], v[4:5], v[6:7]
	v_pk_fma_f32 v[6:7], v[12:13], v[12:13], v[14:15]
	v_pk_mul_f32 v[8:9], v[42:43], v[42:43]
	v_pk_mul_f32 v[10:11], v[44:45], v[44:45]
	v_pk_fma_f32 v[16:17], v[48:49], v[48:49], v[16:17] op_sel_hi:[1,1,0]
	v_pk_fma_f32 v[18:19], v[50:51], v[50:51], v[18:19] op_sel_hi:[1,1,0]
	v_pk_add_f32 v[4:5], v[4:5], v[4:5] op_sel_hi:[0,1]
	v_pk_add_f32 v[6:7], v[6:7], v[6:7] op_sel_hi:[0,1]
	v_mov_b32_e32 v16, v8
	v_mov_b32_e32 v18, v9
	v_mov_b32_e32 v4, v10
	v_mov_b32_e32 v6, v11
	v_pk_add_f32 v[8:9], v[16:17], v[18:19]
	v_pk_add_f32 v[4:5], v[4:5], v[6:7]
	s_nop 0
	v_pk_add_f32 v[4:5], v[8:9], v[4:5]
	s_nop 0
	v_add_f32_e32 v59, v4, v5
	global_load_dwordx4 v[4:7], v2, s[6:7] offset:2048
	global_load_dwordx4 v[8:11], v2, s[8:9] offset:2048
	global_load_dwordx4 v[12:15], v2, s[6:7] offset:3072
	global_load_dwordx4 v[16:19], v2, s[8:9] offset:3072
	v_mov_b32_e32 v53, v59
	s_waitcnt lgkmcnt(0)
	s_nop 1
	v_permlane32_swap_b32_e32 v59, v53
	v_add_f32_e32 v2, v59, v53
	v_mov_b32_e32 v53, v2
	v_mov_b32_e32 v54, 0x3727c5ac
	s_waitcnt lgkmcnt(0)
	s_nop 1
	v_permlane16_swap_b32_e32 v2, v53
	v_add_f32_e32 v2, v2, v53
	v_mov_b32_e32 v55, 0x260
	s_waitcnt lgkmcnt(0)
	s_nop 1
	v_add_f32_dpp v2, v2, v2 row_ror:8 row_mask:0xf bank_mask:0xf
	s_waitcnt lgkmcnt(0)
	s_nop 1
	v_add_f32_dpp v2, v2, v2 row_ror:4 row_mask:0xf bank_mask:0xf
	s_waitcnt lgkmcnt(0)
	s_nop 1
	v_add_f32_dpp v2, v2, v2 row_ror:2 row_mask:0xf bank_mask:0xf
	s_waitcnt lgkmcnt(0)
	s_nop 1
	v_add_f32_dpp v2, v2, v2 row_ror:1 row_mask:0xf bank_mask:0xf
	v_fmac_f32_e32 v54, 0x3a800000, v2
	v_mul_f32_e32 v2, 0x4f800000, v54
	v_cmp_gt_f32_e32 vcc, s0, v54
	s_nop 1
	v_cndmask_b32_e32 v53, v54, v2, vcc
	v_sqrt_f32_e32 v54, v53
	v_lshlrev_b32_e32 v2, 3, v52
	v_lshl_add_u64 v[0:1], v[0:1], 0, v[2:3]
	v_add_u32_e32 v52, -1, v54
	v_add_u32_e32 v56, 1, v54
	v_fma_f32 v57, -v52, v54, v53
	v_fma_f32 v58, -v56, v54, v53
	v_cmp_ge_f32_e64 s[0:1], 0, v57
	s_nop 1
	v_cndmask_b32_e64 v52, v54, v52, s[0:1]
	v_cmp_lt_f32_e64 s[0:1], 0, v58
	s_nop 1
	v_cndmask_b32_e64 v52, v52, v56, s[0:1]
	v_mul_f32_e32 v54, 0x37800000, v52
	v_cndmask_b32_e32 v52, v52, v54, vcc
	v_cmp_class_f32_e32 vcc, v53, v55
	s_nop 1
	v_cndmask_b32_e32 v52, v52, v53, vcc
	v_div_scale_f32 v53, s[0:1], v52, v52, 1.0
	v_rcp_f32_e32 v54, v53
	v_div_scale_f32 v2, vcc, 1.0, v52, 1.0
	v_fma_f32 v3, -v53, v54, 1.0
	v_fmac_f32_e32 v54, v3, v54
	v_mul_f32_e32 v3, v2, v54
	v_fma_f32 v55, -v53, v3, v2
	v_fmac_f32_e32 v3, v55, v54
	v_fma_f32 v2, -v53, v3, v2
	v_div_fmas_f32 v2, v2, v54, v3
	v_div_fixup_f32 v2, v2, v52, 1.0
	v_pk_mul_f32 v[38:39], v[38:39], v[2:3] op_sel_hi:[1,0]
	v_pk_mul_f32 v[40:41], v[40:41], v[2:3] op_sel_hi:[1,0]
	v_pk_mul_f32 v[46:47], v[46:47], v[2:3] op_sel_hi:[1,0]
	v_pk_mul_f32 v[36:37], v[36:37], v[2:3] op_sel_hi:[1,0]
	v_pk_mul_f32 v[48:49], v[48:49], v[2:3] op_sel_hi:[1,0]
	v_pk_mul_f32 v[50:51], v[50:51], v[2:3] op_sel_hi:[1,0]
	v_pk_mul_f32 v[42:43], v[42:43], v[2:3] op_sel_hi:[1,0]
	v_pk_mul_f32 v[2:3], v[44:45], v[2:3] op_sel_hi:[1,0]
	s_waitcnt vmcnt(6)
	v_pk_fma_f32 v[20:21], v[20:21], v[38:39], v[24:25]
	v_pk_fma_f32 v[22:23], v[22:23], v[40:41], v[26:27]
	s_waitcnt vmcnt(4)
	v_pk_fma_f32 v[24:25], v[28:29], v[46:47], v[32:33]
	v_pk_fma_f32 v[26:27], v[30:31], v[36:37], v[34:35]
	s_waitcnt vmcnt(2)
	v_pk_fma_f32 v[4:5], v[48:49], v[4:5], v[8:9]
	v_pk_fma_f32 v[6:7], v[50:51], v[6:7], v[10:11]
	s_waitcnt vmcnt(0)
	v_pk_fma_f32 v[8:9], v[42:43], v[12:13], v[16:17]
	v_pk_fma_f32 v[2:3], v[2:3], v[14:15], v[18:19]
	v_cvt_pk_f16_f32 v10, v20, v21
	v_cvt_pk_f16_f32 v11, v22, v23
	v_cvt_pk_f16_f32 v12, v24, v25
	v_cvt_pk_f16_f32 v13, v26, v27
	v_cvt_pk_f16_f32 v4, v4, v5
	v_cvt_pk_f16_f32 v5, v6, v7
	v_cvt_pk_f16_f32 v6, v8, v9
	v_cvt_pk_f16_f32 v7, v2, v3
	global_store_dwordx2 v[0:1], v[10:11], off
	global_store_dwordx2 v[0:1], v[12:13], off offset:512
	global_store_dwordx2 v[0:1], v[4:5], off offset:1024
	global_store_dwordx2 v[0:1], v[6:7], off offset:1536
	s_endpgm
	s_endpgm
	s_endpgm
	s_endpgm
	s_endpgm
	s_endpgm
	s_endpgm
	s_endpgm
	s_endpgm
	s_endpgm
	s_endpgm
	s_endpgm
	s_endpgm
	s_endpgm
	s_endpgm
	s_endpgm
	s_endpgm
	s_endpgm
	s_endpgm
	s_endpgm
	s_endpgm
	s_endpgm
	s_endpgm
	s_endpgm
	s_endpgm
	s_endpgm
	s_endpgm
	s_endpgm
	s_endpgm
	s_endpgm
	s_endpgm
	s_endpgm
	s_endpgm
	s_endpgm
	s_endpgm
	s_endpgm
	s_endpgm
	s_endpgm
	s_endpgm
	s_endpgm

_Z9ln_kernelILi4EEvPKiPKfS3_PfS3_S3_PDF16_:
	s_load_dwordx8 s[4:11], s[0:1], 0x8
	v_and_b32_e32 v12, 63, v0
	v_lshrrev_b32_e32 v0, 6, v0
	v_lshl_or_b32 v0, s2, 2, v0
	v_ashrrev_i32_e32 v1, 31, v0
	v_lshlrev_b64 v[24:25], 11, v[0:1]
	v_mov_b32_e32 v29, 0
	s_waitcnt lgkmcnt(0)
	v_lshl_add_u64 v[2:3], s[4:5], 0, v[24:25]
	v_lshlrev_b32_e32 v26, 3, v12
	v_mov_b32_e32 v27, v29
	v_lshl_add_u64 v[4:5], v[2:3], 0, v[26:27]
	s_mov_b64 s[2:3], 0x400000
	v_lshl_add_u64 v[10:11], v[4:5], 0, s[2:3]
	global_load_dwordx2 v[6:7], v[4:5], off offset:512
	global_load_dwordx2 v[8:9], v[4:5], off
	global_load_dwordx2 v[46:47], v[10:11], off offset:512
	s_mov_b32 s2, 0x400000
	v_add_co_u32_e32 v2, vcc, s2, v4
	v_lshlrev_b64 v[0:1], 12, v[0:1]
	s_nop 0
	v_addc_co_u32_e32 v3, vcc, 0, v5, vcc
	global_load_dwordx2 v[48:49], v[2:3], off
	v_lshl_add_u64 v[0:1], s[8:9], 0, v[0:1]
	v_lshlrev_b32_e32 v28, 4, v12
	v_lshl_add_u64 v[50:51], v[0:1], 0, v[28:29]
	global_load_dwordx4 v[0:3], v[50:51], off
	global_load_dwordx4 v[34:37], v28, s[6:7] offset:1024
	global_load_dwordx4 v[38:41], v[50:51], off offset:1024
	global_load_dwordx2 v[52:53], v[4:5], off offset:1024
	global_load_dwordx2 v[54:55], v[10:11], off offset:1024
	global_load_dwordx2 v[32:33], v[4:5], off offset:1536
	global_load_dwordx2 v[30:31], v[10:11], off offset:1536
	global_load_dwordx4 v[16:19], v[50:51], off offset:2048
	global_load_dwordx4 v[42:45], v28, s[6:7]
	global_load_dwordx4 v[20:23], v28, s[6:7] offset:2048
	global_load_dwordx4 v[12:15], v[50:51], off offset:3072
	global_load_dwordx4 v[60:63], v28, s[6:7] offset:3072
	s_load_dwordx4 s[4:7], s[0:1], 0x28
	s_mov_b32 s0, 0xf800000
	s_waitcnt lgkmcnt(0)
	v_lshl_add_u64 v[24:25], s[6:7], 0, v[24:25]
	v_lshl_add_u64 v[24:25], v[24:25], 0, v[26:27]
	s_waitcnt vmcnt(15)
	v_cvt_f32_f16_e32 v4, v6
	v_cvt_f32_f16_sdwa v5, v6 dst_sel:DWORD dst_unused:UNUSED_PAD src0_sel:WORD_1
	v_cvt_f32_f16_e32 v56, v7
	v_cvt_f32_f16_sdwa v57, v7 dst_sel:DWORD dst_unused:UNUSED_PAD src0_sel:WORD_1
	s_waitcnt vmcnt(13)
	v_cvt_f32_f16_e32 v6, v46
	v_cvt_f32_f16_sdwa v7, v46 dst_sel:DWORD dst_unused:UNUSED_PAD src0_sel:WORD_1
	v_cvt_f32_f16_e32 v58, v47
	v_cvt_f32_f16_sdwa v59, v47 dst_sel:DWORD dst_unused:UNUSED_PAD src0_sel:WORD_1
	v_cvt_f32_f16_e32 v10, v8
	v_pk_add_f32 v[50:51], v[4:5], v[6:7]
	v_add_f32_e32 v58, v56, v58
	v_add_f32_e32 v57, v57, v59
	s_waitcnt vmcnt(10)
	v_mov_b32_e32 v56, v37
	s_waitcnt vmcnt(9)
	v_pk_add_f32 v[38:39], v[38:39], v[50:51]
	v_add_f32_e32 v37, v40, v58
	v_add_f32_e32 v40, v41, v57
	s_waitcnt vmcnt(8)
	v_cvt_f32_f16_e32 v41, v52
	v_cvt_f32_f16_sdwa v50, v52 dst_sel:DWORD dst_unused:UNUSED_PAD src0_sel:WORD_1
	s_waitcnt vmcnt(7)
	v_cvt_f32_f16_e32 v52, v54
	v_cvt_f32_f16_sdwa v11, v8 dst_sel:DWORD dst_unused:UNUSED_PAD src0_sel:WORD_1
	v_cvt_f32_f16_e32 v46, v48
	v_cvt_f32_f16_sdwa v47, v48 dst_sel:DWORD dst_unused:UNUSED_PAD src0_sel:WORD_1
	v_cvt_f32_f16_e32 v8, v9
	v_cvt_f32_f16_sdwa v9, v9 dst_sel:DWORD dst_unused:UNUSED_PAD src0_sel:WORD_1
	v_cvt_f32_f16_e32 v48, v49
	v_cvt_f32_f16_sdwa v49, v49 dst_sel:DWORD dst_unused:UNUSED_PAD src0_sel:WORD_1
	v_cvt_f32_f16_e32 v51, v53
	v_cvt_f32_f16_sdwa v53, v53 dst_sel:DWORD dst_unused:UNUSED_PAD src0_sel:WORD_1
	v_pk_add_f32 v[34:35], v[34:35], v[38:39]
	v_add_f32_e32 v36, v36, v37
	v_cvt_f32_f16_sdwa v37, v54 dst_sel:DWORD dst_unused:UNUSED_PAD src0_sel:WORD_1
	v_cvt_f32_f16_e32 v38, v55
	v_cvt_f32_f16_sdwa v54, v55 dst_sel:DWORD dst_unused:UNUSED_PAD src0_sel:WORD_1
	s_waitcnt vmcnt(6)
	v_cvt_f32_f16_e32 v39, v32
	v_cvt_f32_f16_sdwa v57, v32 dst_sel:DWORD dst_unused:UNUSED_PAD src0_sel:WORD_1
	v_add_f32_e32 v32, v41, v52
	s_waitcnt vmcnt(4)
	v_add_f32_e32 v16, v16, v32
	v_pk_add_f32 v[46:47], v[10:11], v[46:47]
	s_waitcnt vmcnt(2)
	v_add_f32_e32 v32, v20, v16
	v_mbcnt_lo_u32_b32 v16, -1, 0
	v_pk_add_f32 v[48:49], v[8:9], v[48:49]
	v_pk_add_f32 v[46:47], v[0:1], v[46:47]
	v_add_f32_e32 v38, v51, v38
	v_cvt_f32_f16_e32 v51, v30
	v_cvt_f32_f16_sdwa v41, v30 dst_sel:DWORD dst_unused:UNUSED_PAD src0_sel:WORD_1
	v_add_f32_e32 v30, v53, v54
	v_mbcnt_hi_u32_b32 v54, -1, v16
	v_pk_add_f32 v[48:49], v[2:3], v[48:49]
	v_pk_add_f32 v[42:43], v[42:43], v[46:47]
	v_cvt_f32_f16_e32 v47, v33
	v_cvt_f32_f16_e32 v53, v31
	v_and_b32_e32 v16, 64, v54
	v_pk_add_f32 v[44:45], v[44:45], v[48:49]
	v_cvt_f32_f16_sdwa v49, v33 dst_sel:DWORD dst_unused:UNUSED_PAD src0_sel:WORD_1
	v_cvt_f32_f16_sdwa v31, v31 dst_sel:DWORD dst_unused:UNUSED_PAD src0_sel:WORD_1
	v_add_u32_e32 v55, 64, v16
	v_xor_b32_e32 v16, 32, v54
	v_cmp_lt_i32_e32 vcc, v16, v55
	v_add_f32_e32 v52, v50, v37
	v_add_f32_e32 v18, v18, v38
	v_cndmask_b32_e32 v16, v54, v16, vcc
	v_mov_b32_e32 v46, v17
	v_mov_b32_e32 v38, v44
	v_mov_b32_e32 v50, v45
	v_lshlrev_b32_e32 v58, 2, v16
	v_pk_add_f32 v[16:17], v[46:47], v[52:53]
	v_mov_b32_e32 v20, v21
	s_waitcnt vmcnt(1)
	v_mov_b32_e32 v21, v14
	v_mov_b32_e32 v48, v19
	v_pk_add_f32 v[38:39], v[38:39], v[50:51]
	v_pk_add_f32 v[50:51], v[42:43], v[42:43] op_sel:[0,1] op_sel_hi:[1,0]
	v_pk_add_f32 v[40:41], v[56:57], v[40:41]
	v_pk_add_f32 v[20:21], v[20:21], v[16:17]
	v_pk_add_f32 v[16:17], v[48:49], v[30:31]
	v_mov_b32_e32 v14, v23
	v_mov_b32_e32 v37, v13
	v_pk_add_f32 v[46:47], v[34:35], v[34:35] op_sel:[0,1] op_sel_hi:[1,0]
	v_mov_b32_e32 v51, v12
	v_add_f32_e32 v22, v22, v18
	v_pk_add_f32 v[30:31], v[14:15], v[16:17]
	v_pk_add_f32 v[18:19], v[36:37], v[40:41]
	s_waitcnt vmcnt(0)
	v_mov_b32_e32 v47, v61
	v_mov_b32_e32 v33, v62
	v_mov_b32_e32 v23, v63
	v_pk_add_f32 v[12:13], v[50:51], v[38:39]
	v_mov_b32_e32 v38, v29
	v_mov_b32_e32 v39, v60
	v_pk_add_f32 v[46:47], v[46:47], v[18:19]
	v_pk_add_f32 v[48:49], v[32:33], v[20:21]
	v_pk_add_f32 v[52:53], v[22:23], v[30:31]
	v_pk_add_f32 v[12:13], v[38:39], v[12:13]
	v_pk_add_f32 v[18:19], v[48:49], v[52:53]
	v_pk_add_f32 v[38:39], v[12:13], v[46:47]
	v_mov_b32_e32 v37, v40
	v_pk_add_f32 v[18:19], v[38:39], v[18:19]
	v_mov_b32_e32 v33, v20
	v_add_f32_e32 v12, v18, v19
	v_mov_b32_e32 v18, v12
	v_xor_b32_e32 v19, 16, v54
	v_cmp_lt_i32_e32 vcc, v19, v55
	v_mov_b32_e32 v23, v30
	v_mov_b32_e32 v46, v13
	v_cndmask_b32_e32 v19, v54, v19, vcc
	v_lshlrev_b32_e32 v29, 2, v19
	s_waitcnt lgkmcnt(0)
	s_nop 1
	v_permlane32_swap_b32_e32 v12, v18
	v_add_f32_e32 v12, v12, v18
	v_mov_b32_e32 v18, v12
	v_xor_b32_e32 v19, 8, v54
	v_cmp_lt_i32_e32 vcc, v19, v55
	v_mov_b32_e32 v52, v49
	global_load_dwordx4 v[4:7], v28, s[10:11]
	global_load_dwordx4 v[8:11], v28, s[10:11] offset:1024
	v_cndmask_b32_e32 v19, v54, v19, vcc
	v_lshlrev_b32_e32 v48, 2, v19
	s_waitcnt lgkmcnt(0)
	s_nop 1
	v_permlane16_swap_b32_e32 v12, v18
	v_add_f32_e32 v12, v12, v18
	v_xor_b32_e32 v19, 4, v54
	v_cmp_lt_i32_e32 vcc, v19, v55
	global_load_dwordx4 v[0:3], v28, s[10:11] offset:2048
	global_load_dwordx4 v[14:17], v28, s[10:11] offset:3072
	v_cndmask_b32_e32 v19, v54, v19, vcc
	v_lshlrev_b32_e32 v59, 2, v19
	s_waitcnt lgkmcnt(0)
	s_nop 1
	v_add_f32_dpp v12, v12, v12 row_ror:8 row_mask:0xf bank_mask:0xf
	v_xor_b32_e32 v19, 2, v54
	v_cmp_lt_i32_e32 vcc, v19, v55
	s_waitcnt lgkmcnt(0)
	s_nop 1
	v_add_f32_dpp v12, v12, v12 row_ror:4 row_mask:0xf bank_mask:0xf
	v_cndmask_b32_e32 v19, v54, v19, vcc
	v_lshlrev_b32_e32 v60, 2, v19
	v_xor_b32_e32 v19, 1, v54
	v_cmp_lt_i32_e32 vcc, v19, v55
	s_waitcnt lgkmcnt(0)
	s_nop 1
	v_add_f32_dpp v12, v12, v12 row_ror:2 row_mask:0xf bank_mask:0xf
	v_cndmask_b32_e32 v19, v54, v19, vcc
	v_lshlrev_b32_e32 v61, 2, v19
	s_waitcnt lgkmcnt(0)
	s_nop 1
	v_add_f32_dpp v12, v12, v12 row_ror:1 row_mask:0xf bank_mask:0xf
	v_mul_f32_e32 v12, 0x3a800000, v12
	v_pk_add_f32 v[42:43], v[42:43], v[12:13] op_sel_hi:[1,0] neg_lo:[0,1] neg_hi:[0,1]
	v_pk_add_f32 v[44:45], v[44:45], v[12:13] op_sel_hi:[1,0] neg_lo:[0,1] neg_hi:[0,1]
	v_mov_b32_e32 v38, v43
	v_mov_b32_e32 v39, v45
	v_pk_add_f32 v[50:51], v[34:35], v[12:13] op_sel_hi:[1,0] neg_lo:[0,1] neg_hi:[0,1]
	v_pk_add_f32 v[54:55], v[36:37], v[12:13] op_sel_hi:[1,0] neg_lo:[0,1] neg_hi:[0,1]
	v_pk_add_f32 v[56:57], v[32:33], v[12:13] op_sel_hi:[1,0] neg_lo:[0,1] neg_hi:[0,1]
	v_mov_b32_e32 v18, v42
	v_mov_b32_e32 v19, v44
	v_pk_mul_f32 v[38:39], v[38:39], v[38:39]
	v_mov_b32_e32 v34, v51
	v_mov_b32_e32 v35, v55
	v_mul_f32_e32 v30, v56, v56
	v_pk_fma_f32 v[38:39], v[18:19], v[18:19], v[38:39]
	v_mov_b32_e32 v18, v50
	v_mov_b32_e32 v19, v54
	v_pk_mul_f32 v[34:35], v[34:35], v[34:35]
	v_pk_fma_f32 v[30:31], v[56:57], v[56:57], v[30:31] op_sel_hi:[1,1,0]
	v_pk_add_f32 v[22:23], v[22:23], v[12:13] op_sel_hi:[1,0] neg_lo:[0,1] neg_hi:[0,1]
	v_pk_fma_f32 v[34:35], v[18:19], v[18:19], v[34:35]
	v_mul_f32_e32 v30, v22, v22
	v_pk_add_f32 v[46:47], v[46:47], v[12:13] op_sel_hi:[1,0] neg_lo:[0,1] neg_hi:[0,1]
	v_pk_add_f32 v[12:13], v[52:53], v[12:13] op_sel_hi:[1,0] neg_lo:[0,1] neg_hi:[0,1]
	v_pk_add_f32 v[36:37], v[38:39], v[38:39] op_sel_hi:[0,1]
	v_pk_add_f32 v[34:35], v[34:35], v[34:35] op_sel_hi:[0,1]
	v_pk_fma_f32 v[32:33], v[22:23], v[22:23], v[30:31] op_sel_hi:[1,1,0]
	v_pk_mul_f32 v[38:39], v[46:47], v[46:47]
	v_pk_mul_f32 v[40:41], v[12:13], v[12:13]
	v_mov_b32_e32 v30, v38
	v_mov_b32_e32 v32, v39
	v_mov_b32_e32 v36, v40
	v_mov_b32_e32 v34, v41
	v_pk_add_f32 v[30:31], v[30:31], v[32:33]
	v_pk_add_f32 v[32:33], v[36:37], v[34:35]
	global_load_dwordx4 v[18:21], v28, s[4:5]
	v_pk_add_f32 v[30:31], v[30:31], v[32:33]
	s_nop 0
	v_add_f32_e32 v34, v30, v31
	v_mov_b32_e32 v35, v34
	global_load_dwordx4 v[30:33], v28, s[4:5] offset:1024
	s_waitcnt lgkmcnt(0)
	s_nop 1
	v_permlane32_swap_b32_e32 v34, v35
	v_add_f32_e32 v38, v34, v35
	v_mov_b32_e32 v29, v38
	global_load_dwordx4 v[34:37], v28, s[4:5] offset:2048
	s_waitcnt lgkmcnt(0)
	s_nop 1
	v_permlane16_swap_b32_e32 v38, v29
	v_add_f32_e32 v29, v38, v29
	global_load_dwordx4 v[38:41], v28, s[4:5] offset:3072
	s_waitcnt lgkmcnt(0)
	s_nop 1
	v_add_f32_dpp v28, v29, v29 row_ror:8 row_mask:0xf bank_mask:0xf
	s_waitcnt lgkmcnt(0)
	s_nop 1
	v_add_f32_dpp v28, v28, v28 row_ror:4 row_mask:0xf bank_mask:0xf
	s_waitcnt lgkmcnt(0)
	s_nop 1
	v_add_f32_dpp v28, v28, v28 row_ror:2 row_mask:0xf bank_mask:0xf
	s_waitcnt lgkmcnt(0)
	s_nop 1
	v_add_f32_dpp v28, v28, v28 row_ror:1 row_mask:0xf bank_mask:0xf
	v_mov_b32_e32 v29, 0x3727c5ac
	v_fmac_f32_e32 v29, 0x3a800000, v28
	v_mul_f32_e32 v28, 0x4f800000, v29
	v_cmp_gt_f32_e32 vcc, s0, v29
	s_nop 1
	v_cndmask_b32_e32 v28, v29, v28, vcc
	v_sqrt_f32_e32 v29, v28
	s_nop 0
	v_add_u32_e32 v48, -1, v29
	v_fma_f32 v49, -v48, v29, v28
	v_cmp_ge_f32_e64 s[0:1], 0, v49
	v_add_u32_e32 v49, 1, v29
	s_nop 0
	v_cndmask_b32_e64 v48, v29, v48, s[0:1]
	v_fma_f32 v29, -v49, v29, v28
	v_cmp_lt_f32_e64 s[0:1], 0, v29
	s_nop 1
	v_cndmask_b32_e64 v29, v48, v49, s[0:1]
	v_mul_f32_e32 v48, 0x37800000, v29
	v_cndmask_b32_e32 v29, v29, v48, vcc
	v_mov_b32_e32 v48, 0x260
	v_cmp_class_f32_e32 vcc, v28, v48
	s_nop 1
	v_cndmask_b32_e32 v28, v29, v28, vcc
	v_div_scale_f32 v29, s[0:1], v28, v28, 1.0
	v_rcp_f32_e32 v48, v29
	s_nop 0
	v_fma_f32 v26, -v29, v48, 1.0
	v_fmac_f32_e32 v48, v26, v48
	v_div_scale_f32 v26, vcc, 1.0, v28, 1.0
	v_mul_f32_e32 v27, v26, v48
	v_fma_f32 v49, -v29, v27, v26
	v_fmac_f32_e32 v27, v49, v48
	v_fma_f32 v26, -v29, v27, v26
	v_div_fmas_f32 v26, v26, v48, v27
	v_div_fixup_f32 v26, v26, v28, 1.0
	v_pk_mul_f32 v[28:29], v[42:43], v[26:27] op_sel_hi:[1,0]
	s_waitcnt vmcnt(3)
	v_pk_fma_f32 v[4:5], v[4:5], v[28:29], v[18:19]
	v_pk_mul_f32 v[18:19], v[44:45], v[26:27] op_sel_hi:[1,0]
	v_cvt_pk_f16_f32 v4, v4, v5
	v_pk_fma_f32 v[6:7], v[6:7], v[18:19], v[20:21]
	s_nop 0
	v_cvt_pk_f16_f32 v5, v6, v7
	global_store_dwordx2 v[24:25], v[4:5], off
	v_pk_mul_f32 v[4:5], v[50:51], v[26:27] op_sel_hi:[1,0]
	v_pk_mul_f32 v[6:7], v[54:55], v[26:27] op_sel_hi:[1,0]
	s_waitcnt vmcnt(3)
	v_pk_fma_f32 v[4:5], v[8:9], v[4:5], v[30:31]
	v_pk_fma_f32 v[6:7], v[10:11], v[6:7], v[32:33]
	v_cvt_pk_f16_f32 v4, v4, v5
	v_cvt_pk_f16_f32 v5, v6, v7
	global_store_dwordx2 v[24:25], v[4:5], off offset:512
	v_pk_mul_f32 v[4:5], v[56:57], v[26:27] op_sel_hi:[1,0]
	s_waitcnt vmcnt(3)
	v_pk_fma_f32 v[0:1], v[0:1], v[4:5], v[34:35]
	v_pk_mul_f32 v[4:5], v[22:23], v[26:27] op_sel_hi:[1,0]
	v_cvt_pk_f16_f32 v0, v0, v1
	v_pk_fma_f32 v[2:3], v[4:5], v[2:3], v[36:37]
	s_nop 0
	v_cvt_pk_f16_f32 v1, v2, v3
	global_store_dwordx2 v[24:25], v[0:1], off offset:1024
	v_pk_mul_f32 v[0:1], v[46:47], v[26:27] op_sel_hi:[1,0]
	v_pk_mul_f32 v[2:3], v[12:13], v[26:27] op_sel_hi:[1,0]
	s_waitcnt vmcnt(3)
	v_pk_fma_f32 v[0:1], v[0:1], v[14:15], v[38:39]
	v_pk_fma_f32 v[2:3], v[2:3], v[16:17], v[40:41]
	v_cvt_pk_f16_f32 v0, v0, v1
	v_cvt_pk_f16_f32 v1, v2, v3
	global_store_dwordx2 v[24:25], v[0:1], off offset:1536
	s_endpgm
	s_endpgm
	s_endpgm
	s_endpgm
	s_endpgm
	s_endpgm
	s_endpgm
	s_endpgm
	s_endpgm
	s_endpgm
	s_endpgm
	s_endpgm
	s_endpgm
	s_endpgm
	s_endpgm
	s_endpgm
	s_endpgm
	s_endpgm
	s_endpgm
